# stack14 plus rowmax cross-half exchange moved into the rare rescale blocks, code size of every region kept equal modulo 8 bytes
# speedup vs baseline: 1.0004x; 1.0004x over previous
; #define AT_SBAR() __builtin_amdgcn_sched_barrier(0)
; template <int OFF> DI s16x4 tr_read(int vb) { s16x4 r; asm volatile("ds_read_b64_tr_b16 %0, %1 offset:%2" : "=&v"(r) : "v"(vb), "i"(OFF) : "memory"); return r; }
; template <int D0> DI void pv_one(f32x16& od, int vb, bf16x8 pa0, bf16x8 pa1, bf16x8 pa2, bf16x8 pa3) {
;     const s16x4 l0 = tr_read<v_rd_off(D0, 0, 0)>(vb), h0 = tr_read<v_rd_off(D0, 0, 1)>(vb), l1 = tr_read<v_rd_off(D0, 1, 0)>(vb), h1 = tr_read<v_rd_off(D0, 1, 1)>(vb);
;     const s16x4 l2 = tr_read<v_rd_off(D0, 2, 0)>(vb), h2 = tr_read<v_rd_off(D0, 2, 1)>(vb), l3 = tr_read<v_rd_off(D0, 3, 0)>(vb), h3 = tr_read<v_rd_off(D0, 3, 1)>(vb);
;     asm volatile("s_waitcnt lgkmcnt(0)" ::: "memory"); AT_SBAR();
;     ...
;     od = __builtin_amdgcn_mfma_f32_32x32x16_bf16(AT_PK(l0, h0), pa0, od, 0, 0, 0);
;     od = __builtin_amdgcn_mfma_f32_32x32x16_bf16(AT_PK(l1, h1), pa1, od, 0, 0, 0);
;     od = __builtin_amdgcn_mfma_f32_32x32x16_bf16(AT_PK(l2, h2), pa2, od, 0, 0, 0);
;     od = __builtin_amdgcn_mfma_f32_32x32x16_bf16(AT_PK(l3, h3), pa3, od, 0, 0, 0);
;     ...
; }
; DI void pv_all_sm(f32x16* o, int vb, bf16x8 pa0, bf16x8 pa1, bf16x8 pa2, bf16x8 pa3, f32x16& p0, f32x16& p1, float& m_ref, f32x16& negm, float& alpha) {
;     pv_one<0>(o[0], vb, pa0, pa1, pa2, pa3);
;     float pmax = p0[0];
; #pragma unroll
;     for (int r = 1; r < 16; ++r) pmax = fmaxf(pmax, p0[r]);
;     pv_one<1>(o[1], vb, pa0, pa1, pa2, pa3);
; #pragma unroll
;     for (int r = 0; r < 16; ++r) pmax = fmaxf(pmax, p1[r]);
;     { auto rr = __builtin_amdgcn_permlane32_swap(__float_as_uint(pmax), __float_as_uint(pmax), false, false); pmax = fmaxf(__uint_as_float(rr[0]), __uint_as_float(rr[1])); }
;     pv_one<2>(o[2], vb, pa0, pa1, pa2, pa3);
;     alpha = 1.f;
;     if (__builtin_expect(!__all(pmax <= THRL), 0)) {
;         const float dl = fmaxf(pmax, 0.f); m_ref += dl; alpha = __builtin_amdgcn_exp2f(-dl);
; #pragma unroll
;         for (int r = 0; r < 16; ++r) { p0[r] -= dl; p1[r] -= dl; }
; #pragma unroll
;         for (int r = 0; r < 16; ++r) negm[r] = -m_ref;
;     }
.LBB4_704:
	s_lshl_b32 s67, s65, 14
	v_add_u32_e32 v186, s67, v253
	ds_read_b64_tr_b16 v[64:65], v186 offset:0
	ds_read_b64_tr_b16 v[66:67], v186 offset:0x100
	ds_read_b64_tr_b16 v[68:69], v186 offset:0x1000
	ds_read_b64_tr_b16 v[70:71], v186 offset:0x1100
	ds_read_b64_tr_b16 v[72:73], v186 offset:0x2000
	ds_read_b64_tr_b16 v[74:75], v186 offset:0x2100
	ds_read_b64_tr_b16 v[76:77], v186 offset:0x3000
	ds_read_b64_tr_b16 v[78:79], v186 offset:0x3100
	s_waitcnt lgkmcnt(0)
	v_mfma_f32_32x32x16_bf16 v[32:47], v[64:67], v[96:99], v[32:47]
	v_max_f32_e32 v64, v128, v129
	v_max3_f32 v64, v64, v130, v131
	v_max3_f32 v64, v64, v132, v133
	v_max3_f32 v64, v64, v134, v135
	v_max3_f32 v64, v64, v136, v137
	v_mfma_f32_32x32x16_bf16 v[32:47], v[68:71], v[108:111], v[32:47]
	v_max3_f32 v64, v64, v138, v139
	v_max3_f32 v66, v64, v140, v141
	ds_read_b64_tr_b16 v[64:65], v186 offset:0x200
	v_max3_f32 v180, v66, v142, v143
	ds_read_b64_tr_b16 v[66:67], v186 offset:0x300
	ds_read_b64_tr_b16 v[68:69], v186 offset:0x1200
	ds_read_b64_tr_b16 v[70:71], v186 offset:0x1300
	v_mfma_f32_32x32x16_bf16 v[32:47], v[72:75], v[100:103], v[32:47]
	ds_read_b64_tr_b16 v[72:73], v186 offset:0x2200
	ds_read_b64_tr_b16 v[74:75], v186 offset:0x2300
	ds_read_b64_tr_b16 v[214:215], v186 offset:0x3200
	ds_read_b64_tr_b16 v[216:217], v186 offset:0x3300
	v_mfma_f32_32x32x16_bf16 v[32:47], v[76:79], v[104:107], v[32:47]
	s_waitcnt lgkmcnt(0)
	v_mfma_f32_32x32x16_bf16 v[48:63], v[64:67], v[96:99], v[48:63]
	v_max3_f32 v76, v180, v112, v113
	v_max3_f32 v64, v76, v114, v115
	ds_read_b64_tr_b16 v[66:67], v186 offset:0x400
	v_max3_f32 v64, v64, v116, v117
	v_max3_f32 v64, v64, v118, v119
	v_max3_f32 v64, v64, v120, v121
	v_max3_f32 v64, v64, v122, v123
	v_mfma_f32_32x32x16_bf16 v[48:63], v[68:71], v[108:111], v[48:63]
	ds_read_b64_tr_b16 v[68:69], v186 offset:0x500
	ds_read_b64_tr_b16 v[70:71], v186 offset:0x1400
	v_max3_f32 v64, v64, v124, v125
	v_max3_f32 v64, v64, v126, v127
	v_cmp_ge_f32_e32 vcc, s25, v64
	v_mfma_f32_32x32x16_bf16 v[48:63], v[72:75], v[100:103], v[48:63]
	ds_read_b64_tr_b16 v[72:73], v186 offset:0x1500
	ds_read_b64_tr_b16 v[74:75], v186 offset:0x2400
	ds_read_b64_tr_b16 v[76:77], v186 offset:0x2500
	ds_read_b64_tr_b16 v[218:219], v186 offset:0x3400
	ds_read_b64_tr_b16 v[220:221], v186 offset:0x3500
	v_mfma_f32_32x32x16_bf16 v[48:63], v[214:217], v[104:107], v[48:63]
	s_waitcnt lgkmcnt(0)
	s_cmp_eq_u64 vcc, exec
	v_mfma_f32_32x32x16_bf16 v[16:31], v[66:69], v[96:99], v[16:31]
	v_mfma_f32_32x32x16_bf16 v[16:31], v[70:73], v[108:111], v[16:31]
	v_mfma_f32_32x32x16_bf16 v[16:31], v[74:77], v[100:103], v[16:31]
	v_mfma_f32_32x32x16_bf16 v[16:31], v[218:221], v[104:107], v[16:31]
	s_cbranch_scc0 .LBB4_737
	v_mov_b32_e32 v180, 1.0

; #define AT_SBAR() __builtin_amdgcn_sched_barrier(0)
; template <int OFF> DI s16x4 tr_read(int vb) { s16x4 r; asm volatile("ds_read_b64_tr_b16 %0, %1 offset:%2" : "=&v"(r) : "v"(vb), "i"(OFF) : "memory"); return r; }
; template <int D0> DI void pv_one(f32x16& od, int vb, bf16x8 pa0, bf16x8 pa1, bf16x8 pa2, bf16x8 pa3) {
;     const s16x4 l0 = tr_read<v_rd_off(D0, 0, 0)>(vb), h0 = tr_read<v_rd_off(D0, 0, 1)>(vb), l1 = tr_read<v_rd_off(D0, 1, 0)>(vb), h1 = tr_read<v_rd_off(D0, 1, 1)>(vb);
;     const s16x4 l2 = tr_read<v_rd_off(D0, 2, 0)>(vb), h2 = tr_read<v_rd_off(D0, 2, 1)>(vb), l3 = tr_read<v_rd_off(D0, 3, 0)>(vb), h3 = tr_read<v_rd_off(D0, 3, 1)>(vb);
;     asm volatile("s_waitcnt lgkmcnt(0)" ::: "memory"); AT_SBAR();
;     ...
;     od = __builtin_amdgcn_mfma_f32_32x32x16_bf16(AT_PK(l0, h0), pa0, od, 0, 0, 0);
;     od = __builtin_amdgcn_mfma_f32_32x32x16_bf16(AT_PK(l1, h1), pa1, od, 0, 0, 0);
;     od = __builtin_amdgcn_mfma_f32_32x32x16_bf16(AT_PK(l2, h2), pa2, od, 0, 0, 0);
;     od = __builtin_amdgcn_mfma_f32_32x32x16_bf16(AT_PK(l3, h3), pa3, od, 0, 0, 0);
;     ...
; }
; DI void pv_all_sm(f32x16* o, int vb, bf16x8 pa0, bf16x8 pa1, bf16x8 pa2, bf16x8 pa3, f32x16& p0, f32x16& p1, float& m_ref, f32x16& negm, float& alpha) {
;     pv_one<0>(o[0], vb, pa0, pa1, pa2, pa3);
;     float pmax = p0[0];
; #pragma unroll
;     for (int r = 1; r < 16; ++r) pmax = fmaxf(pmax, p0[r]);
;     pv_one<1>(o[1], vb, pa0, pa1, pa2, pa3);
; #pragma unroll
;     for (int r = 0; r < 16; ++r) pmax = fmaxf(pmax, p1[r]);
;     { auto rr = __builtin_amdgcn_permlane32_swap(__float_as_uint(pmax), __float_as_uint(pmax), false, false); pmax = fmaxf(__uint_as_float(rr[0]), __uint_as_float(rr[1])); }
;     pv_one<2>(o[2], vb, pa0, pa1, pa2, pa3);
;     alpha = 1.f;
;     if (__builtin_expect(!__all(pmax <= THRL), 0)) {
;         const float dl = fmaxf(pmax, 0.f); m_ref += dl; alpha = __builtin_amdgcn_exp2f(-dl);
; #pragma unroll
;         for (int r = 0; r < 16; ++r) { p0[r] -= dl; p1[r] -= dl; }
; #pragma unroll
;         for (int r = 0; r < 16; ++r) negm[r] = -m_ref;
;     }
.LBB4_725:
	v_lshl_add_u32 v215, s66, 14, v253
	ds_read_b64_tr_b16 v[216:217], v215 offset:0
	ds_read_b64_tr_b16 v[218:219], v215 offset:0x100
	ds_read_b64_tr_b16 v[220:221], v215 offset:0x1000
	ds_read_b64_tr_b16 v[222:223], v215 offset:0x1100
	ds_read_b64_tr_b16 v[224:225], v215 offset:0x2000
	ds_read_b64_tr_b16 v[226:227], v215 offset:0x2100
	ds_read_b64_tr_b16 v[228:229], v215 offset:0x3000
	ds_read_b64_tr_b16 v[230:231], v215 offset:0x3100
	s_waitcnt lgkmcnt(0)
	v_mfma_f32_32x32x16_bf16 v[32:47], v[216:219], v[120:123], v[32:47]
	v_max_f32_e32 v186, v128, v129
	ds_read_b64_tr_b16 v[216:217], v215 offset:0x200
	ds_read_b64_tr_b16 v[218:219], v215 offset:0x300
	v_max3_f32 v186, v186, v130, v131
	v_max3_f32 v186, v186, v132, v133
	v_mfma_f32_32x32x16_bf16 v[32:47], v[220:223], v[124:127], v[32:47]
	ds_read_b64_tr_b16 v[220:221], v215 offset:0x1200
	ds_read_b64_tr_b16 v[222:223], v215 offset:0x1300
	v_max3_f32 v186, v186, v134, v135
	v_max3_f32 v186, v186, v136, v137
	v_max3_f32 v186, v186, v138, v139
	v_max3_f32 v186, v186, v140, v141
	v_max3_f32 v186, v186, v142, v143
	v_mfma_f32_32x32x16_bf16 v[32:47], v[224:227], v[112:115], v[32:47]
	ds_read_b64_tr_b16 v[224:225], v215 offset:0x2200
	ds_read_b64_tr_b16 v[226:227], v215 offset:0x2300
	ds_read_b64_tr_b16 v[232:233], v215 offset:0x3200
	ds_read_b64_tr_b16 v[234:235], v215 offset:0x3300
	v_mfma_f32_32x32x16_bf16 v[32:47], v[228:231], v[116:119], v[32:47]
	s_waitcnt lgkmcnt(0)
	v_mfma_f32_32x32x16_bf16 v[48:63], v[216:219], v[120:123], v[48:63]
	v_max3_f32 v186, v186, v96, v97
	v_max3_f32 v186, v186, v98, v99
	ds_read_b64_tr_b16 v[218:219], v215 offset:0x400
	v_max3_f32 v186, v186, v100, v101
	v_max3_f32 v186, v186, v102, v103
	v_max3_f32 v186, v186, v104, v105
	v_max3_f32 v186, v186, v106, v107
	v_mfma_f32_32x32x16_bf16 v[48:63], v[220:223], v[124:127], v[48:63]
	ds_read_b64_tr_b16 v[220:221], v215 offset:0x500
	ds_read_b64_tr_b16 v[222:223], v215 offset:0x1400
	v_max3_f32 v186, v186, v108, v109
	v_max3_f32 v186, v186, v110, v111
	v_cmp_ge_f32_e32 vcc, s25, v186
	v_mfma_f32_32x32x16_bf16 v[48:63], v[224:227], v[112:115], v[48:63]
	ds_read_b64_tr_b16 v[224:225], v215 offset:0x1500
	ds_read_b64_tr_b16 v[226:227], v215 offset:0x2400
	ds_read_b64_tr_b16 v[228:229], v215 offset:0x2500
	ds_read_b64_tr_b16 v[236:237], v215 offset:0x3400
	ds_read_b64_tr_b16 v[238:239], v215 offset:0x3500
	v_mfma_f32_32x32x16_bf16 v[48:63], v[232:235], v[116:119], v[48:63]
	s_waitcnt lgkmcnt(0)
	v_mov_b32_e32 v216, v186
	v_mfma_f32_32x32x16_bf16 v[16:31], v[218:221], v[120:123], v[16:31]
	s_cmp_eq_u64 vcc, exec
	v_mov_b32_e64 v186, 1.0
	v_mfma_f32_32x32x16_bf16 v[16:31], v[222:225], v[124:127], v[16:31]
	v_mfma_f32_32x32x16_bf16 v[16:31], v[226:229], v[112:115], v[16:31]
	v_mfma_f32_32x32x16_bf16 v[16:31], v[236:239], v[116:119], v[16:31]
	s_cbranch_scc0 .LBB4_738

; #define AT_SBAR() __builtin_amdgcn_sched_barrier(0)
; template <int OFF> DI s16x4 tr_read(int vb) { s16x4 r; asm volatile("ds_read_b64_tr_b16 %0, %1 offset:%2" : "=&v"(r) : "v"(vb), "i"(OFF) : "memory"); return r; }
; template <int D0> DI void pv_one(f32x16& od, int vb, bf16x8 pa0, bf16x8 pa1, bf16x8 pa2, bf16x8 pa3) {
;     const s16x4 l0 = tr_read<v_rd_off(D0, 0, 0)>(vb), h0 = tr_read<v_rd_off(D0, 0, 1)>(vb), l1 = tr_read<v_rd_off(D0, 1, 0)>(vb), h1 = tr_read<v_rd_off(D0, 1, 1)>(vb);
;     const s16x4 l2 = tr_read<v_rd_off(D0, 2, 0)>(vb), h2 = tr_read<v_rd_off(D0, 2, 1)>(vb), l3 = tr_read<v_rd_off(D0, 3, 0)>(vb), h3 = tr_read<v_rd_off(D0, 3, 1)>(vb);
;     asm volatile("s_waitcnt lgkmcnt(0)" ::: "memory"); AT_SBAR();
;     ...
;     od = __builtin_amdgcn_mfma_f32_32x32x16_bf16(AT_PK(l0, h0), pa0, od, 0, 0, 0);
;     od = __builtin_amdgcn_mfma_f32_32x32x16_bf16(AT_PK(l1, h1), pa1, od, 0, 0, 0);
;     od = __builtin_amdgcn_mfma_f32_32x32x16_bf16(AT_PK(l2, h2), pa2, od, 0, 0, 0);
;     od = __builtin_amdgcn_mfma_f32_32x32x16_bf16(AT_PK(l3, h3), pa3, od, 0, 0, 0);
;     ...
; }
; DI void pv_all_sm(f32x16* o, int vb, bf16x8 pa0, bf16x8 pa1, bf16x8 pa2, bf16x8 pa3, f32x16& p0, f32x16& p1, float& m_ref, f32x16& negm, float& alpha) {
;     pv_one<0>(o[0], vb, pa0, pa1, pa2, pa3);
;     float pmax = p0[0];
; #pragma unroll
;     for (int r = 1; r < 16; ++r) pmax = fmaxf(pmax, p0[r]);
;     pv_one<1>(o[1], vb, pa0, pa1, pa2, pa3);
; #pragma unroll
;     for (int r = 0; r < 16; ++r) pmax = fmaxf(pmax, p1[r]);
;     { auto rr = __builtin_amdgcn_permlane32_swap(__float_as_uint(pmax), __float_as_uint(pmax), false, false); pmax = fmaxf(__uint_as_float(rr[0]), __uint_as_float(rr[1])); }
;     pv_one<2>(o[2], vb, pa0, pa1, pa2, pa3);
;     alpha = 1.f;
;     if (__builtin_expect(!__all(pmax <= THRL), 0)) {
;         const float dl = fmaxf(pmax, 0.f); m_ref += dl; alpha = __builtin_amdgcn_exp2f(-dl);
; #pragma unroll
;         for (int r = 0; r < 16; ++r) { p0[r] -= dl; p1[r] -= dl; }
; #pragma unroll
;         for (int r = 0; r < 16; ++r) negm[r] = -m_ref;
;     }
.LBB4_777:
	s_lshl_b32 s31, s29, 14
	v_add_u32_e32 v182, s31, v253
	ds_read_b64_tr_b16 v[64:65], v182 offset:0
	ds_read_b64_tr_b16 v[66:67], v182 offset:0x100
	ds_read_b64_tr_b16 v[68:69], v182 offset:0x1000
	ds_read_b64_tr_b16 v[70:71], v182 offset:0x1100
	ds_read_b64_tr_b16 v[72:73], v182 offset:0x2000
	ds_read_b64_tr_b16 v[74:75], v182 offset:0x2100
	ds_read_b64_tr_b16 v[76:77], v182 offset:0x3000
	ds_read_b64_tr_b16 v[78:79], v182 offset:0x3100
	s_waitcnt lgkmcnt(0)
	v_mfma_f32_32x32x16_bf16 v[48:63], v[64:67], v[96:99], v[48:63]
	v_max_f32_e32 v64, v128, v129
	v_max3_f32 v64, v64, v130, v131
	v_max3_f32 v64, v64, v132, v133
	v_max3_f32 v64, v64, v134, v135
	v_max3_f32 v64, v64, v136, v137
	v_mfma_f32_32x32x16_bf16 v[48:63], v[68:71], v[108:111], v[48:63]
	v_max3_f32 v64, v64, v138, v139
	v_max3_f32 v66, v64, v140, v141
	ds_read_b64_tr_b16 v[64:65], v182 offset:0x200
	v_max3_f32 v180, v66, v142, v143
	ds_read_b64_tr_b16 v[66:67], v182 offset:0x300
	ds_read_b64_tr_b16 v[68:69], v182 offset:0x1200
	ds_read_b64_tr_b16 v[70:71], v182 offset:0x1300
	v_mfma_f32_32x32x16_bf16 v[48:63], v[72:75], v[100:103], v[48:63]
	ds_read_b64_tr_b16 v[72:73], v182 offset:0x2200
	ds_read_b64_tr_b16 v[74:75], v182 offset:0x2300
	ds_read_b64_tr_b16 v[218:219], v182 offset:0x3200
	ds_read_b64_tr_b16 v[220:221], v182 offset:0x3300
	v_mfma_f32_32x32x16_bf16 v[48:63], v[76:79], v[104:107], v[48:63]
	s_waitcnt lgkmcnt(0)
	v_mfma_f32_32x32x16_bf16 v[32:47], v[64:67], v[96:99], v[32:47]
	v_max3_f32 v76, v180, v112, v113
	v_max3_f32 v64, v76, v114, v115
	ds_read_b64_tr_b16 v[66:67], v182 offset:0x400
	v_max3_f32 v64, v64, v116, v117
	v_max3_f32 v64, v64, v118, v119
	v_max3_f32 v64, v64, v120, v121
	v_max3_f32 v64, v64, v122, v123
	v_mfma_f32_32x32x16_bf16 v[32:47], v[68:71], v[108:111], v[32:47]
	ds_read_b64_tr_b16 v[68:69], v182 offset:0x500
	ds_read_b64_tr_b16 v[70:71], v182 offset:0x1400
	v_max3_f32 v64, v64, v124, v125
	v_max3_f32 v64, v64, v126, v127
	v_cmp_ge_f32_e32 vcc, s26, v64
	v_mfma_f32_32x32x16_bf16 v[32:47], v[72:75], v[100:103], v[32:47]
	ds_read_b64_tr_b16 v[72:73], v182 offset:0x1500
	ds_read_b64_tr_b16 v[74:75], v182 offset:0x2400
	ds_read_b64_tr_b16 v[76:77], v182 offset:0x2500
	ds_read_b64_tr_b16 v[222:223], v182 offset:0x3400
	ds_read_b64_tr_b16 v[224:225], v182 offset:0x3500
	v_mfma_f32_32x32x16_bf16 v[32:47], v[218:221], v[104:107], v[32:47]
	s_waitcnt lgkmcnt(0)
	s_cmp_eq_u64 vcc, exec
	v_mfma_f32_32x32x16_bf16 v[16:31], v[66:69], v[96:99], v[16:31]
	v_mfma_f32_32x32x16_bf16 v[16:31], v[70:73], v[108:111], v[16:31]
	v_mfma_f32_32x32x16_bf16 v[16:31], v[74:77], v[100:103], v[16:31]
	v_mfma_f32_32x32x16_bf16 v[16:31], v[222:225], v[104:107], v[16:31]
	s_cbranch_scc0 .LBB4_810
	v_mov_b32_e32 v180, 1.0

; #define AT_SBAR() __builtin_amdgcn_sched_barrier(0)
; template <int OFF> DI s16x4 tr_read(int vb) { s16x4 r; asm volatile("ds_read_b64_tr_b16 %0, %1 offset:%2" : "=&v"(r) : "v"(vb), "i"(OFF) : "memory"); return r; }
; template <int D0> DI void pv_one(f32x16& od, int vb, bf16x8 pa0, bf16x8 pa1, bf16x8 pa2, bf16x8 pa3) {
;     const s16x4 l0 = tr_read<v_rd_off(D0, 0, 0)>(vb), h0 = tr_read<v_rd_off(D0, 0, 1)>(vb), l1 = tr_read<v_rd_off(D0, 1, 0)>(vb), h1 = tr_read<v_rd_off(D0, 1, 1)>(vb);
;     const s16x4 l2 = tr_read<v_rd_off(D0, 2, 0)>(vb), h2 = tr_read<v_rd_off(D0, 2, 1)>(vb), l3 = tr_read<v_rd_off(D0, 3, 0)>(vb), h3 = tr_read<v_rd_off(D0, 3, 1)>(vb);
;     asm volatile("s_waitcnt lgkmcnt(0)" ::: "memory"); AT_SBAR();
;     ...
;     od = __builtin_amdgcn_mfma_f32_32x32x16_bf16(AT_PK(l0, h0), pa0, od, 0, 0, 0);
;     od = __builtin_amdgcn_mfma_f32_32x32x16_bf16(AT_PK(l1, h1), pa1, od, 0, 0, 0);
;     od = __builtin_amdgcn_mfma_f32_32x32x16_bf16(AT_PK(l2, h2), pa2, od, 0, 0, 0);
;     od = __builtin_amdgcn_mfma_f32_32x32x16_bf16(AT_PK(l3, h3), pa3, od, 0, 0, 0);
;     ...
; }
; DI void pv_all_sm(f32x16* o, int vb, bf16x8 pa0, bf16x8 pa1, bf16x8 pa2, bf16x8 pa3, f32x16& p0, f32x16& p1, float& m_ref, f32x16& negm, float& alpha) {
;     pv_one<0>(o[0], vb, pa0, pa1, pa2, pa3);
;     float pmax = p0[0];
; #pragma unroll
;     for (int r = 1; r < 16; ++r) pmax = fmaxf(pmax, p0[r]);
;     pv_one<1>(o[1], vb, pa0, pa1, pa2, pa3);
; #pragma unroll
;     for (int r = 0; r < 16; ++r) pmax = fmaxf(pmax, p1[r]);
;     { auto rr = __builtin_amdgcn_permlane32_swap(__float_as_uint(pmax), __float_as_uint(pmax), false, false); pmax = fmaxf(__uint_as_float(rr[0]), __uint_as_float(rr[1])); }
;     pv_one<2>(o[2], vb, pa0, pa1, pa2, pa3);
;     alpha = 1.f;
;     if (__builtin_expect(!__all(pmax <= THRL), 0)) {
;         const float dl = fmaxf(pmax, 0.f); m_ref += dl; alpha = __builtin_amdgcn_exp2f(-dl);
; #pragma unroll
;         for (int r = 0; r < 16; ++r) { p0[r] -= dl; p1[r] -= dl; }
; #pragma unroll
;         for (int r = 0; r < 16; ++r) negm[r] = -m_ref;
;     }
.LBB4_798:
	v_lshl_add_u32 v219, s30, 14, v253
	ds_read_b64_tr_b16 v[220:221], v219 offset:0
	ds_read_b64_tr_b16 v[222:223], v219 offset:0x100
	ds_read_b64_tr_b16 v[224:225], v219 offset:0x1000
	ds_read_b64_tr_b16 v[226:227], v219 offset:0x1100
	ds_read_b64_tr_b16 v[228:229], v219 offset:0x2000
	ds_read_b64_tr_b16 v[230:231], v219 offset:0x2100
	ds_read_b64_tr_b16 v[232:233], v219 offset:0x3000
	ds_read_b64_tr_b16 v[234:235], v219 offset:0x3100
	s_waitcnt lgkmcnt(0)
	v_mfma_f32_32x32x16_bf16 v[48:63], v[220:223], v[120:123], v[48:63]
	v_max_f32_e32 v182, v128, v129
	ds_read_b64_tr_b16 v[220:221], v219 offset:0x200
	ds_read_b64_tr_b16 v[222:223], v219 offset:0x300
	v_max3_f32 v182, v182, v130, v131
	v_max3_f32 v182, v182, v132, v133
	v_mfma_f32_32x32x16_bf16 v[48:63], v[224:227], v[124:127], v[48:63]
	ds_read_b64_tr_b16 v[224:225], v219 offset:0x1200
	ds_read_b64_tr_b16 v[226:227], v219 offset:0x1300
	v_max3_f32 v182, v182, v134, v135
	v_max3_f32 v182, v182, v136, v137
	v_max3_f32 v182, v182, v138, v139
	v_max3_f32 v182, v182, v140, v141
	v_max3_f32 v182, v182, v142, v143
	v_mfma_f32_32x32x16_bf16 v[48:63], v[228:231], v[112:115], v[48:63]
	ds_read_b64_tr_b16 v[228:229], v219 offset:0x2200
	ds_read_b64_tr_b16 v[230:231], v219 offset:0x2300
	ds_read_b64_tr_b16 v[236:237], v219 offset:0x3200
	ds_read_b64_tr_b16 v[238:239], v219 offset:0x3300
	v_mfma_f32_32x32x16_bf16 v[48:63], v[232:235], v[116:119], v[48:63]
	s_waitcnt lgkmcnt(0)
	v_mfma_f32_32x32x16_bf16 v[32:47], v[220:223], v[120:123], v[32:47]
	v_max3_f32 v182, v182, v96, v97
	v_max3_f32 v182, v182, v98, v99
	ds_read_b64_tr_b16 v[222:223], v219 offset:0x400
	v_max3_f32 v182, v182, v100, v101
	v_max3_f32 v182, v182, v102, v103
	v_max3_f32 v182, v182, v104, v105
	v_max3_f32 v182, v182, v106, v107
	v_mfma_f32_32x32x16_bf16 v[32:47], v[224:227], v[124:127], v[32:47]
	ds_read_b64_tr_b16 v[224:225], v219 offset:0x500
	ds_read_b64_tr_b16 v[226:227], v219 offset:0x1400
	v_max3_f32 v182, v182, v108, v109
	v_max3_f32 v182, v182, v110, v111
	v_cmp_ge_f32_e32 vcc, s26, v182
	v_mfma_f32_32x32x16_bf16 v[32:47], v[228:231], v[112:115], v[32:47]
	ds_read_b64_tr_b16 v[228:229], v219 offset:0x1500
	ds_read_b64_tr_b16 v[230:231], v219 offset:0x2400
	ds_read_b64_tr_b16 v[232:233], v219 offset:0x2500
	ds_read_b64_tr_b16 v[240:241], v219 offset:0x3400
	ds_read_b64_tr_b16 v[242:243], v219 offset:0x3500
	v_mfma_f32_32x32x16_bf16 v[32:47], v[236:239], v[116:119], v[32:47]
	s_waitcnt lgkmcnt(0)
	v_mov_b32_e32 v220, v182
	v_mfma_f32_32x32x16_bf16 v[16:31], v[222:225], v[120:123], v[16:31]
	s_cmp_eq_u64 vcc, exec
	v_mov_b32_e64 v182, 1.0
	v_mfma_f32_32x32x16_bf16 v[16:31], v[226:229], v[124:127], v[16:31]
	v_mfma_f32_32x32x16_bf16 v[16:31], v[230:233], v[112:115], v[16:31]
	v_mfma_f32_32x32x16_bf16 v[16:31], v[240:243], v[116:119], v[16:31]
	s_cbranch_scc0 .LBB4_811

; #define AT_SBAR() __builtin_amdgcn_sched_barrier(0)
; template <int OFF> DI s16x4 tr_read(int vb) { s16x4 r; asm volatile("ds_read_b64_tr_b16 %0, %1 offset:%2" : "=&v"(r) : "v"(vb), "i"(OFF) : "memory"); return r; }
; template <int D0> DI void pv_one(f32x16& od, int vb, bf16x8 pa0, bf16x8 pa1, bf16x8 pa2, bf16x8 pa3) {
;     const s16x4 l0 = tr_read<v_rd_off(D0, 0, 0)>(vb), h0 = tr_read<v_rd_off(D0, 0, 1)>(vb), l1 = tr_read<v_rd_off(D0, 1, 0)>(vb), h1 = tr_read<v_rd_off(D0, 1, 1)>(vb);
;     const s16x4 l2 = tr_read<v_rd_off(D0, 2, 0)>(vb), h2 = tr_read<v_rd_off(D0, 2, 1)>(vb), l3 = tr_read<v_rd_off(D0, 3, 0)>(vb), h3 = tr_read<v_rd_off(D0, 3, 1)>(vb);
;     asm volatile("s_waitcnt lgkmcnt(0)" ::: "memory"); AT_SBAR();
;     ...
;     od = __builtin_amdgcn_mfma_f32_32x32x16_bf16(AT_PK(l0, h0), pa0, od, 0, 0, 0);
;     od = __builtin_amdgcn_mfma_f32_32x32x16_bf16(AT_PK(l1, h1), pa1, od, 0, 0, 0);
;     od = __builtin_amdgcn_mfma_f32_32x32x16_bf16(AT_PK(l2, h2), pa2, od, 0, 0, 0);
;     od = __builtin_amdgcn_mfma_f32_32x32x16_bf16(AT_PK(l3, h3), pa3, od, 0, 0, 0);
;     ...
; }
; DI void pv_all_sm(f32x16* o, int vb, bf16x8 pa0, bf16x8 pa1, bf16x8 pa2, bf16x8 pa3, f32x16& p0, f32x16& p1, float& m_ref, f32x16& negm, float& alpha) {
;     pv_one<0>(o[0], vb, pa0, pa1, pa2, pa3);
;     float pmax = p0[0];
; #pragma unroll
;     for (int r = 1; r < 16; ++r) pmax = fmaxf(pmax, p0[r]);
;     pv_one<1>(o[1], vb, pa0, pa1, pa2, pa3);
; #pragma unroll
;     for (int r = 0; r < 16; ++r) pmax = fmaxf(pmax, p1[r]);
;     { auto rr = __builtin_amdgcn_permlane32_swap(__float_as_uint(pmax), __float_as_uint(pmax), false, false); pmax = fmaxf(__uint_as_float(rr[0]), __uint_as_float(rr[1])); }
;     pv_one<2>(o[2], vb, pa0, pa1, pa2, pa3);
;     alpha = 1.f;
;     if (__builtin_expect(!__all(pmax <= THRL), 0)) {
;         const float dl = fmaxf(pmax, 0.f); m_ref += dl; alpha = __builtin_amdgcn_exp2f(-dl);
; #pragma unroll
;         for (int r = 0; r < 16; ++r) { p0[r] -= dl; p1[r] -= dl; }
; #pragma unroll
;         for (int r = 0; r < 16; ++r) negm[r] = -m_ref;
;     }
.LBB4_851:
	s_lshl_b32 s65, s63, 14
	v_add_u32_e32 v182, s65, v253
	ds_read_b64_tr_b16 v[64:65], v182 offset:0
	ds_read_b64_tr_b16 v[66:67], v182 offset:0x100
	ds_read_b64_tr_b16 v[68:69], v182 offset:0x1000
	ds_read_b64_tr_b16 v[70:71], v182 offset:0x1100
	ds_read_b64_tr_b16 v[72:73], v182 offset:0x2000
	ds_read_b64_tr_b16 v[74:75], v182 offset:0x2100
	ds_read_b64_tr_b16 v[76:77], v182 offset:0x3000
	ds_read_b64_tr_b16 v[78:79], v182 offset:0x3100
	s_waitcnt lgkmcnt(0)
	v_mfma_f32_32x32x16_bf16 v[32:47], v[64:67], v[96:99], v[32:47]
	v_max_f32_e32 v64, v128, v129
	v_max3_f32 v64, v64, v130, v131
	v_max3_f32 v64, v64, v132, v133
	v_max3_f32 v64, v64, v134, v135
	v_max3_f32 v64, v64, v136, v137
	v_mfma_f32_32x32x16_bf16 v[32:47], v[68:71], v[108:111], v[32:47]
	v_max3_f32 v64, v64, v138, v139
	v_max3_f32 v66, v64, v140, v141
	ds_read_b64_tr_b16 v[64:65], v182 offset:0x200
	v_max3_f32 v180, v66, v142, v143
	ds_read_b64_tr_b16 v[66:67], v182 offset:0x300
	ds_read_b64_tr_b16 v[68:69], v182 offset:0x1200
	ds_read_b64_tr_b16 v[70:71], v182 offset:0x1300
	v_mfma_f32_32x32x16_bf16 v[32:47], v[72:75], v[100:103], v[32:47]
	ds_read_b64_tr_b16 v[72:73], v182 offset:0x2200
	ds_read_b64_tr_b16 v[74:75], v182 offset:0x2300
	ds_read_b64_tr_b16 v[214:215], v182 offset:0x3200
	ds_read_b64_tr_b16 v[216:217], v182 offset:0x3300
	v_mfma_f32_32x32x16_bf16 v[32:47], v[76:79], v[104:107], v[32:47]
	s_waitcnt lgkmcnt(0)
	v_mfma_f32_32x32x16_bf16 v[48:63], v[64:67], v[96:99], v[48:63]
	v_max3_f32 v76, v180, v112, v113
	v_max3_f32 v64, v76, v114, v115
	ds_read_b64_tr_b16 v[66:67], v182 offset:0x400
	v_max3_f32 v64, v64, v116, v117
	v_max3_f32 v64, v64, v118, v119
	v_max3_f32 v64, v64, v120, v121
	v_max3_f32 v64, v64, v122, v123
	v_mfma_f32_32x32x16_bf16 v[48:63], v[68:71], v[108:111], v[48:63]
	ds_read_b64_tr_b16 v[68:69], v182 offset:0x500
	ds_read_b64_tr_b16 v[70:71], v182 offset:0x1400
	v_max3_f32 v64, v64, v124, v125
	v_max3_f32 v64, v64, v126, v127
	v_cmp_ge_f32_e32 vcc, s15, v64
	v_mfma_f32_32x32x16_bf16 v[48:63], v[72:75], v[100:103], v[48:63]
	ds_read_b64_tr_b16 v[72:73], v182 offset:0x1500
	ds_read_b64_tr_b16 v[74:75], v182 offset:0x2400
	ds_read_b64_tr_b16 v[76:77], v182 offset:0x2500
	ds_read_b64_tr_b16 v[218:219], v182 offset:0x3400
	ds_read_b64_tr_b16 v[220:221], v182 offset:0x3500
	v_mfma_f32_32x32x16_bf16 v[48:63], v[214:217], v[104:107], v[48:63]
	s_waitcnt lgkmcnt(0)
	s_cmp_eq_u64 vcc, exec
	v_mfma_f32_32x32x16_bf16 v[16:31], v[66:69], v[96:99], v[16:31]
	v_mfma_f32_32x32x16_bf16 v[16:31], v[70:73], v[108:111], v[16:31]
	v_mfma_f32_32x32x16_bf16 v[16:31], v[74:77], v[100:103], v[16:31]
	v_mfma_f32_32x32x16_bf16 v[16:31], v[218:221], v[104:107], v[16:31]
	s_cbranch_scc0 .LBB4_884
	v_mov_b32_e32 v180, 1.0

; #define AT_SBAR() __builtin_amdgcn_sched_barrier(0)
; template <int OFF> DI s16x4 tr_read(int vb) { s16x4 r; asm volatile("ds_read_b64_tr_b16 %0, %1 offset:%2" : "=&v"(r) : "v"(vb), "i"(OFF) : "memory"); return r; }
; template <int D0> DI void pv_one(f32x16& od, int vb, bf16x8 pa0, bf16x8 pa1, bf16x8 pa2, bf16x8 pa3) {
;     const s16x4 l0 = tr_read<v_rd_off(D0, 0, 0)>(vb), h0 = tr_read<v_rd_off(D0, 0, 1)>(vb), l1 = tr_read<v_rd_off(D0, 1, 0)>(vb), h1 = tr_read<v_rd_off(D0, 1, 1)>(vb);
;     const s16x4 l2 = tr_read<v_rd_off(D0, 2, 0)>(vb), h2 = tr_read<v_rd_off(D0, 2, 1)>(vb), l3 = tr_read<v_rd_off(D0, 3, 0)>(vb), h3 = tr_read<v_rd_off(D0, 3, 1)>(vb);
;     asm volatile("s_waitcnt lgkmcnt(0)" ::: "memory"); AT_SBAR();
;     ...
;     od = __builtin_amdgcn_mfma_f32_32x32x16_bf16(AT_PK(l0, h0), pa0, od, 0, 0, 0);
;     od = __builtin_amdgcn_mfma_f32_32x32x16_bf16(AT_PK(l1, h1), pa1, od, 0, 0, 0);
;     od = __builtin_amdgcn_mfma_f32_32x32x16_bf16(AT_PK(l2, h2), pa2, od, 0, 0, 0);
;     od = __builtin_amdgcn_mfma_f32_32x32x16_bf16(AT_PK(l3, h3), pa3, od, 0, 0, 0);
;     ...
; }
; DI void pv_all_sm(f32x16* o, int vb, bf16x8 pa0, bf16x8 pa1, bf16x8 pa2, bf16x8 pa3, f32x16& p0, f32x16& p1, float& m_ref, f32x16& negm, float& alpha) {
;     pv_one<0>(o[0], vb, pa0, pa1, pa2, pa3);
;     float pmax = p0[0];
; #pragma unroll
;     for (int r = 1; r < 16; ++r) pmax = fmaxf(pmax, p0[r]);
;     pv_one<1>(o[1], vb, pa0, pa1, pa2, pa3);
; #pragma unroll
;     for (int r = 0; r < 16; ++r) pmax = fmaxf(pmax, p1[r]);
;     { auto rr = __builtin_amdgcn_permlane32_swap(__float_as_uint(pmax), __float_as_uint(pmax), false, false); pmax = fmaxf(__uint_as_float(rr[0]), __uint_as_float(rr[1])); }
;     pv_one<2>(o[2], vb, pa0, pa1, pa2, pa3);
;     alpha = 1.f;
;     if (__builtin_expect(!__all(pmax <= THRL), 0)) {
;         const float dl = fmaxf(pmax, 0.f); m_ref += dl; alpha = __builtin_amdgcn_exp2f(-dl);
; #pragma unroll
;         for (int r = 0; r < 16; ++r) { p0[r] -= dl; p1[r] -= dl; }
; #pragma unroll
;         for (int r = 0; r < 16; ++r) negm[r] = -m_ref;
;     }
.LBB4_872:
	v_lshl_add_u32 v215, s64, 14, v253
	ds_read_b64_tr_b16 v[216:217], v215 offset:0
	ds_read_b64_tr_b16 v[218:219], v215 offset:0x100
	ds_read_b64_tr_b16 v[220:221], v215 offset:0x1000
	ds_read_b64_tr_b16 v[222:223], v215 offset:0x1100
	ds_read_b64_tr_b16 v[224:225], v215 offset:0x2000
	ds_read_b64_tr_b16 v[226:227], v215 offset:0x2100
	ds_read_b64_tr_b16 v[228:229], v215 offset:0x3000
	ds_read_b64_tr_b16 v[230:231], v215 offset:0x3100
	s_waitcnt lgkmcnt(0)
	v_mfma_f32_32x32x16_bf16 v[32:47], v[216:219], v[120:123], v[32:47]
	v_max_f32_e32 v182, v128, v129
	ds_read_b64_tr_b16 v[216:217], v215 offset:0x200
	ds_read_b64_tr_b16 v[218:219], v215 offset:0x300
	v_max3_f32 v182, v182, v130, v131
	v_max3_f32 v182, v182, v132, v133
	v_mfma_f32_32x32x16_bf16 v[32:47], v[220:223], v[124:127], v[32:47]
	ds_read_b64_tr_b16 v[220:221], v215 offset:0x1200
	ds_read_b64_tr_b16 v[222:223], v215 offset:0x1300
	v_max3_f32 v182, v182, v134, v135
	v_max3_f32 v182, v182, v136, v137
	v_max3_f32 v182, v182, v138, v139
	v_max3_f32 v182, v182, v140, v141
	v_max3_f32 v182, v182, v142, v143
	v_mfma_f32_32x32x16_bf16 v[32:47], v[224:227], v[112:115], v[32:47]
	ds_read_b64_tr_b16 v[224:225], v215 offset:0x2200
	ds_read_b64_tr_b16 v[226:227], v215 offset:0x2300
	ds_read_b64_tr_b16 v[232:233], v215 offset:0x3200
	ds_read_b64_tr_b16 v[234:235], v215 offset:0x3300
	v_mfma_f32_32x32x16_bf16 v[32:47], v[228:231], v[116:119], v[32:47]
	s_waitcnt lgkmcnt(0)
	v_mfma_f32_32x32x16_bf16 v[48:63], v[216:219], v[120:123], v[48:63]
	v_max3_f32 v182, v182, v96, v97
	v_max3_f32 v182, v182, v98, v99
	ds_read_b64_tr_b16 v[218:219], v215 offset:0x400
	v_max3_f32 v182, v182, v100, v101
	v_max3_f32 v182, v182, v102, v103
	v_max3_f32 v182, v182, v104, v105
	v_max3_f32 v182, v182, v106, v107
	v_mfma_f32_32x32x16_bf16 v[48:63], v[220:223], v[124:127], v[48:63]
	ds_read_b64_tr_b16 v[220:221], v215 offset:0x500
	ds_read_b64_tr_b16 v[222:223], v215 offset:0x1400
	v_max3_f32 v182, v182, v108, v109
	v_max3_f32 v182, v182, v110, v111
	v_cmp_ge_f32_e32 vcc, s15, v182
	v_mfma_f32_32x32x16_bf16 v[48:63], v[224:227], v[112:115], v[48:63]
	ds_read_b64_tr_b16 v[224:225], v215 offset:0x1500
	ds_read_b64_tr_b16 v[226:227], v215 offset:0x2400
	ds_read_b64_tr_b16 v[228:229], v215 offset:0x2500
	ds_read_b64_tr_b16 v[236:237], v215 offset:0x3400
	ds_read_b64_tr_b16 v[238:239], v215 offset:0x3500
	v_mfma_f32_32x32x16_bf16 v[48:63], v[232:235], v[116:119], v[48:63]
	s_waitcnt lgkmcnt(0)
	v_mov_b32_e32 v216, v182
	v_mfma_f32_32x32x16_bf16 v[16:31], v[218:221], v[120:123], v[16:31]
	s_cmp_eq_u64 vcc, exec
	v_mov_b32_e64 v182, 1.0
	v_mfma_f32_32x32x16_bf16 v[16:31], v[222:225], v[124:127], v[16:31]
	v_mfma_f32_32x32x16_bf16 v[16:31], v[226:229], v[112:115], v[16:31]
	v_mfma_f32_32x32x16_bf16 v[16:31], v[236:239], v[116:119], v[16:31]
	s_cbranch_scc0 .LBB4_885
